# v049 + down-projection epilogues (both layers): the 8 per-row-group gate loads issued together up front with counted vmcnt waits instead of a load/vmcnt(0)/store ladder
# speedup vs baseline: 1.0092x; 1.0036x over previous
; __device__ __forceinline__ u32x4 pack8(const f32x4 a, const f32x4 b) { u32x4 w; w.x = cvt_pk_bf16(a[0], a[1]); w.y = cvt_pk_bf16(a[2], a[3]); w.z = cvt_pk_bf16(b[0], b[1]); w.w = cvt_pk_bf16(b[2], b[3]); return w; }
;     __device__ __forceinline__ void operator()(const f32x4 (&acc)[2][2][4][2], const Unit& u, int wr, int wc, int fr, int fq) const {
;     ...
; #pragma unroll
;         for (int ai = 0; ai < 2; ++ai)
; #pragma unroll
;             for (int m = 0; m < 4; ++m) { const int row = row0 + ai * HALF + m * 16; const float gsc = gvp[row];
; #pragma unroll
;                 for (int bj = 0; bj < 2; ++bj) *(u32x4*)(base + (size_t)row * D + col0 + bj * HALF) = pack8(acc[ai][bj][m][0] * gsc, acc[ai][bj][m][1] * gsc); }
.LBB0_1110:
	s_mul_i32 s6, s57, 0x480000
	s_mul_hi_i32 s7, s57, 0x480000
	s_add_u32 s6, s84, s6
	s_mul_i32 s8, s57, 0x900
	s_addc_u32 s7, s85, s7
	s_ashr_i32 s9, s8, 31
	s_lshl_b64 s[8:9], s[8:9], 2
	s_add_u32 s8, s96, s8
	v_lshl_add_u32 v4, s58, 8, v1
	s_addc_u32 s9, s97, s9
	s_andn2_b64 vcc, exec, s[4:5]
	v_lshl_or_b32 v134, s56, 8, v217
	s_cbranch_vccnz .LBB0_1112
	v_ashrrev_i32_e32 v5, 31, v4
	v_lshl_add_u64 v[138:139], v[4:5], 2, s[8:9]
	global_load_dword v162, v[138:139], off
	global_load_dword v164, v[138:139], off offset:64
	global_load_dword v174, v[138:139], off offset:128
	global_load_dword v176, v[138:139], off offset:192
	global_load_dword v178, v[138:139], off offset:512
	global_load_dword v180, v[138:139], off offset:576
	global_load_dword v190, v[138:139], off offset:640
	global_load_dword v192, v[138:139], off offset:704
	v_ashrrev_i32_e32 v135, 31, v134
	v_lshl_add_u64 v[148:149], v[134:135], 1, s[6:7]
	v_lshlrev_b64 v[136:137], 11, v[4:5]
	v_lshl_add_u64 v[136:137], v[148:149], 0, v[136:137]
	s_mov_b32 s18, 0x40000
	s_mov_b64 s[4:5], 0x40000
	s_waitcnt vmcnt(7)
	v_pk_mul_f32 v[142:143], v[68:69], v[162:163] op_sel_hi:[1,0]
	v_pk_mul_f32 v[144:145], v[66:67], v[162:163] op_sel_hi:[1,0]
	v_pk_mul_f32 v[146:147], v[64:65], v[162:163] op_sel_hi:[1,0]
	v_pk_mul_f32 v[150:151], v[62:63], v[162:163] op_sel_hi:[1,0]
	v_pk_mul_f32 v[152:153], v[60:61], v[162:163] op_sel_hi:[1,0]
	v_pk_mul_f32 v[154:155], v[58:59], v[162:163] op_sel_hi:[1,0]
	v_pk_mul_f32 v[156:157], v[56:57], v[162:163] op_sel_hi:[1,0]
	v_pk_mul_f32 v[158:159], v[54:55], v[162:163] op_sel_hi:[1,0]
	v_cvt_pk_bf16_f32 v140, v144, v145
	v_cvt_pk_bf16_f32 v141, v142, v143
	v_cvt_pk_bf16_f32 v142, v150, v151
	v_cvt_pk_bf16_f32 v143, v146, v147
	v_cvt_pk_bf16_f32 v144, v154, v155
	v_cvt_pk_bf16_f32 v145, v152, v153
	v_cvt_pk_bf16_f32 v146, v158, v159
	v_cvt_pk_bf16_f32 v147, v156, v157
	global_store_dwordx4 v[136:137], v[140:143], off
	global_store_dwordx4 v[136:137], v[144:147], off offset:256
	v_or_b32_e32 v142, 16, v4
	v_ashrrev_i32_e32 v143, 31, v142
	v_lshlrev_b64 v[142:143], 11, v[142:143]
	v_lshl_add_u64 v[150:151], v[148:149], 0, v[142:143]
	s_waitcnt vmcnt(8)
	v_pk_mul_f32 v[142:143], v[52:53], v[164:165] op_sel_hi:[1,0]
	v_pk_mul_f32 v[144:145], v[50:51], v[164:165] op_sel_hi:[1,0]
	v_pk_mul_f32 v[146:147], v[48:49], v[164:165] op_sel_hi:[1,0]
	v_pk_mul_f32 v[152:153], v[46:47], v[164:165] op_sel_hi:[1,0]
	v_pk_mul_f32 v[154:155], v[44:45], v[164:165] op_sel_hi:[1,0]
	v_pk_mul_f32 v[156:157], v[42:43], v[164:165] op_sel_hi:[1,0]
	v_pk_mul_f32 v[158:159], v[40:41], v[164:165] op_sel_hi:[1,0]
	v_pk_mul_f32 v[160:161], v[38:39], v[164:165] op_sel_hi:[1,0]
	v_cvt_pk_bf16_f32 v140, v144, v145
	v_cvt_pk_bf16_f32 v141, v142, v143
	v_cvt_pk_bf16_f32 v142, v152, v153
	v_cvt_pk_bf16_f32 v143, v146, v147
	v_cvt_pk_bf16_f32 v144, v156, v157
	v_cvt_pk_bf16_f32 v145, v154, v155
	v_cvt_pk_bf16_f32 v146, v160, v161
	v_cvt_pk_bf16_f32 v147, v158, v159
	global_store_dwordx4 v[150:151], v[140:143], off
	global_store_dwordx4 v[150:151], v[144:147], off offset:256
	v_or_b32_e32 v142, 32, v4
	v_ashrrev_i32_e32 v143, 31, v142
	v_lshlrev_b64 v[142:143], 11, v[142:143]
	v_lshl_add_u64 v[150:151], v[148:149], 0, v[142:143]
	s_waitcnt vmcnt(9)
	v_pk_mul_f32 v[142:143], v[36:37], v[174:175] op_sel_hi:[1,0]
	v_pk_mul_f32 v[144:145], v[34:35], v[174:175] op_sel_hi:[1,0]
	v_pk_mul_f32 v[146:147], v[32:33], v[174:175] op_sel_hi:[1,0]
	v_pk_mul_f32 v[152:153], v[30:31], v[174:175] op_sel_hi:[1,0]
	v_pk_mul_f32 v[154:155], v[28:29], v[174:175] op_sel_hi:[1,0]
	v_pk_mul_f32 v[156:157], v[26:27], v[174:175] op_sel_hi:[1,0]
	v_pk_mul_f32 v[158:159], v[24:25], v[174:175] op_sel_hi:[1,0]
	v_pk_mul_f32 v[160:161], v[22:23], v[174:175] op_sel_hi:[1,0]
	v_cvt_pk_bf16_f32 v140, v144, v145
	v_cvt_pk_bf16_f32 v141, v142, v143
	v_cvt_pk_bf16_f32 v142, v152, v153
	v_cvt_pk_bf16_f32 v143, v146, v147
	v_cvt_pk_bf16_f32 v144, v156, v157
	v_cvt_pk_bf16_f32 v145, v154, v155
	v_cvt_pk_bf16_f32 v146, v160, v161
	v_cvt_pk_bf16_f32 v147, v158, v159
	global_store_dwordx4 v[150:151], v[140:143], off
	global_store_dwordx4 v[150:151], v[144:147], off offset:256
	v_or_b32_e32 v142, 48, v4
	v_ashrrev_i32_e32 v143, 31, v142
	v_lshlrev_b64 v[142:143], 11, v[142:143]
	v_lshl_add_u64 v[148:149], v[148:149], 0, v[142:143]
	s_waitcnt vmcnt(10)
; __device__ __forceinline__ u32x4 pack8(const f32x4 a, const f32x4 b) { u32x4 w; w.x = cvt_pk_bf16(a[0], a[1]); w.y = cvt_pk_bf16(a[2], a[3]); w.z = cvt_pk_bf16(b[0], b[1]); w.w = cvt_pk_bf16(b[2], b[3]); return w; }
;     __device__ __forceinline__ void operator()(const f32x4 (&acc)[2][2][4][2], const Unit& u, int wr, int wc, int fr, int fq) const {
;     ...
; #pragma unroll
;         for (int ai = 0; ai < 2; ++ai)
; #pragma unroll
;             for (int m = 0; m < 4; ++m) { const int row = row0 + ai * HALF + m * 16; const float gsc = gvp[row];
; #pragma unroll
;                 for (int bj = 0; bj < 2; ++bj) *(u32x4*)(base + (size_t)row * D + col0 + bj * HALF) = pack8(acc[ai][bj][m][0] * gsc, acc[ai][bj][m][1] * gsc); }
	v_pk_mul_f32 v[142:143], v[20:21], v[176:177] op_sel_hi:[1,0]
	v_pk_mul_f32 v[144:145], v[18:19], v[176:177] op_sel_hi:[1,0]
	v_pk_mul_f32 v[146:147], v[16:17], v[176:177] op_sel_hi:[1,0]
	v_pk_mul_f32 v[150:151], v[14:15], v[176:177] op_sel_hi:[1,0]
	v_pk_mul_f32 v[152:153], v[12:13], v[176:177] op_sel_hi:[1,0]
	v_pk_mul_f32 v[154:155], v[10:11], v[176:177] op_sel_hi:[1,0]
	v_pk_mul_f32 v[156:157], v[8:9], v[176:177] op_sel_hi:[1,0]
	v_pk_mul_f32 v[158:159], v[6:7], v[176:177] op_sel_hi:[1,0]
	v_cvt_pk_bf16_f32 v140, v144, v145
	v_cvt_pk_bf16_f32 v141, v142, v143
	v_cvt_pk_bf16_f32 v142, v150, v151
	v_cvt_pk_bf16_f32 v143, v146, v147
	v_cvt_pk_bf16_f32 v144, v154, v155
	v_cvt_pk_bf16_f32 v145, v152, v153
	v_cvt_pk_bf16_f32 v146, v158, v159
	v_cvt_pk_bf16_f32 v147, v156, v157
	global_store_dwordx4 v[148:149], v[140:143], off
	global_store_dwordx4 v[148:149], v[144:147], off offset:256
	v_lshl_add_u64 v[142:143], v[136:137], 0, s[4:5]
	v_add_co_u32_e32 v144, vcc, s18, v136
	s_mov_b32 s18, 0x48000
	s_nop 0
	v_addc_co_u32_e32 v145, vcc, 0, v137, vcc
	s_mov_b64 s[4:5], 0x48000
	s_waitcnt vmcnt(11)
	v_pk_mul_f32 v[132:133], v[132:133], v[178:179] op_sel_hi:[1,0]
	v_pk_mul_f32 v[130:131], v[130:131], v[178:179] op_sel_hi:[1,0]
	v_pk_mul_f32 v[128:129], v[128:129], v[178:179] op_sel_hi:[1,0]
	v_pk_mul_f32 v[126:127], v[126:127], v[178:179] op_sel_hi:[1,0]
	v_pk_mul_f32 v[124:125], v[124:125], v[178:179] op_sel_hi:[1,0]
	v_pk_mul_f32 v[122:123], v[122:123], v[178:179] op_sel_hi:[1,0]
	v_pk_mul_f32 v[146:147], v[120:121], v[178:179] op_sel_hi:[1,0]
	v_pk_mul_f32 v[140:141], v[118:119], v[178:179] op_sel_hi:[1,0]
	v_cvt_pk_bf16_f32 v118, v130, v131
	v_cvt_pk_bf16_f32 v119, v132, v133
	v_cvt_pk_bf16_f32 v120, v126, v127
	v_cvt_pk_bf16_f32 v121, v128, v129
	v_cvt_pk_bf16_f32 v122, v122, v123
	v_cvt_pk_bf16_f32 v123, v124, v125
	v_cvt_pk_bf16_f32 v124, v140, v141
	v_cvt_pk_bf16_f32 v125, v146, v147
	global_store_dwordx4 v[144:145], v[118:121], off
	global_store_dwordx4 v[142:143], v[122:125], off offset:256
	v_lshl_add_u64 v[120:121], v[136:137], 0, s[4:5]
	v_add_co_u32_e32 v122, vcc, s18, v136
	s_mov_b64 s[4:5], 0x50000
	s_nop 0
	v_addc_co_u32_e32 v123, vcc, 0, v137, vcc
	s_waitcnt vmcnt(12)
	v_pk_mul_f32 v[116:117], v[116:117], v[180:181] op_sel_hi:[1,0]
	v_pk_mul_f32 v[114:115], v[114:115], v[180:181] op_sel_hi:[1,0]
	v_pk_mul_f32 v[112:113], v[112:113], v[180:181] op_sel_hi:[1,0]
	v_pk_mul_f32 v[110:111], v[110:111], v[180:181] op_sel_hi:[1,0]
	v_pk_mul_f32 v[108:109], v[108:109], v[180:181] op_sel_hi:[1,0]
	v_pk_mul_f32 v[106:107], v[106:107], v[180:181] op_sel_hi:[1,0]
	v_pk_mul_f32 v[124:125], v[104:105], v[180:181] op_sel_hi:[1,0]
	v_pk_mul_f32 v[118:119], v[102:103], v[180:181] op_sel_hi:[1,0]
	v_cvt_pk_bf16_f32 v102, v114, v115
	v_cvt_pk_bf16_f32 v103, v116, v117
	v_cvt_pk_bf16_f32 v104, v110, v111
	v_cvt_pk_bf16_f32 v105, v112, v113
	v_cvt_pk_bf16_f32 v106, v106, v107
	v_cvt_pk_bf16_f32 v107, v108, v109
	v_cvt_pk_bf16_f32 v108, v118, v119
	v_cvt_pk_bf16_f32 v109, v124, v125
	global_store_dwordx4 v[122:123], v[102:105], off
	global_store_dwordx4 v[120:121], v[106:109], off offset:256
	v_lshl_add_u64 v[104:105], v[136:137], 0, s[4:5]
	v_add_co_u32_e32 v106, vcc, s50, v136
	s_mov_b64 s[4:5], -1
	s_nop 0
	v_addc_co_u32_e32 v107, vcc, 0, v137, vcc
	s_waitcnt vmcnt(13)
	v_pk_mul_f32 v[100:101], v[100:101], v[190:191] op_sel_hi:[1,0]
	v_pk_mul_f32 v[98:99], v[98:99], v[190:191] op_sel_hi:[1,0]
	v_pk_mul_f32 v[96:97], v[96:97], v[190:191] op_sel_hi:[1,0]
	v_pk_mul_f32 v[94:95], v[94:95], v[190:191] op_sel_hi:[1,0]
	v_pk_mul_f32 v[92:93], v[92:93], v[190:191] op_sel_hi:[1,0]
	v_pk_mul_f32 v[90:91], v[90:91], v[190:191] op_sel_hi:[1,0]
	v_pk_mul_f32 v[108:109], v[88:89], v[190:191] op_sel_hi:[1,0]
	v_pk_mul_f32 v[102:103], v[86:87], v[190:191] op_sel_hi:[1,0]
	v_cvt_pk_bf16_f32 v86, v98, v99
	v_cvt_pk_bf16_f32 v87, v100, v101
	v_cvt_pk_bf16_f32 v88, v94, v95
	v_cvt_pk_bf16_f32 v89, v96, v97
	v_cvt_pk_bf16_f32 v90, v90, v91
	v_cvt_pk_bf16_f32 v91, v92, v93
	v_cvt_pk_bf16_f32 v92, v102, v103
	v_cvt_pk_bf16_f32 v93, v108, v109
	global_store_dwordx4 v[106:107], v[86:89], off
	global_store_dwordx4 v[104:105], v[90:93], off offset:256
	v_lshl_add_u64 v[86:87], v[136:137], 0, s[12:13]
	v_add_co_u32_e32 v90, vcc, s51, v136
	s_waitcnt vmcnt(14)
	v_pk_mul_f32 v[84:85], v[84:85], v[192:193] op_sel_hi:[1,0]
	v_pk_mul_f32 v[82:83], v[82:83], v[192:193] op_sel_hi:[1,0]
	v_pk_mul_f32 v[92:93], v[80:81], v[192:193] op_sel_hi:[1,0]
	v_pk_mul_f32 v[80:81], v[78:79], v[192:193] op_sel_hi:[1,0]
	v_addc_co_u32_e32 v91, vcc, 0, v137, vcc
	v_pk_mul_f32 v[76:77], v[76:77], v[192:193] op_sel_hi:[1,0]
	v_pk_mul_f32 v[74:75], v[74:75], v[192:193] op_sel_hi:[1,0]
	v_pk_mul_f32 v[72:73], v[72:73], v[192:193] op_sel_hi:[1,0]
	v_pk_mul_f32 v[70:71], v[70:71], v[192:193] op_sel_hi:[1,0]
	v_cvt_pk_bf16_f32 v78, v82, v83
	v_cvt_pk_bf16_f32 v79, v84, v85
	v_cvt_pk_bf16_f32 v80, v80, v81
	v_cvt_pk_bf16_f32 v81, v92, v93
	global_store_dwordx4 v[90:91], v[78:81], off
	s_cbranch_execz .LBB0_1113
	s_branch .LBB0_1115

; __device__ __forceinline__ u32x4 pack8(const f32x4 a, const f32x4 b) { u32x4 w; w.x = cvt_pk_bf16(a[0], a[1]); w.y = cvt_pk_bf16(a[2], a[3]); w.z = cvt_pk_bf16(b[0], b[1]); w.w = cvt_pk_bf16(b[2], b[3]); return w; }
;     __device__ __forceinline__ void operator()(const f32x4 (&acc)[2][2][4][2], const Unit& u, int wr, int wc, int fr, int fq) const {
;     ...
; #pragma unroll
;         for (int ai = 0; ai < 2; ++ai)
; #pragma unroll
;             for (int m = 0; m < 4; ++m) { const int row = row0 + ai * HALF + m * 16; const float gsc = gvp[row];
; #pragma unroll
;                 for (int bj = 0; bj < 2; ++bj) *(u32x4*)(base + (size_t)row * D + col0 + bj * HALF) = pack8(acc[ai][bj][m][0] * gsc, acc[ai][bj][m][1] * gsc); }
.LBB0_2414:
	s_mul_i32 s18, s51, 0x480000
	s_mul_hi_i32 s19, s51, 0x480000
	s_add_u32 s18, s84, s18
	s_mul_i32 s20, s51, 0x900
	s_addc_u32 s19, s85, s19
	s_ashr_i32 s21, s20, 31
	s_lshl_b64 s[20:21], s[20:21], 2
	v_lshl_add_u32 v168, s53, 8, v1
	s_add_u32 s20, s96, s20
	s_addc_u32 s21, s97, s21
	v_ashrrev_i32_e32 v169, 31, v168
	v_lshl_add_u64 v[148:149], v[168:169], 2, s[20:21]
	global_load_dword v176, v[148:149], off
	global_load_dword v178, v[148:149], off offset:64
	global_load_dword v180, v[148:149], off offset:128
	global_load_dword v182, v[148:149], off offset:192
	global_load_dword v184, v[148:149], off offset:512
	global_load_dword v186, v[148:149], off offset:576
	global_load_dword v188, v[148:149], off offset:640
	global_load_dword v190, v[148:149], off offset:704
	v_lshl_or_b32 v146, s52, 8, v152
	v_ashrrev_i32_e32 v147, 31, v146
	v_lshlrev_b64 v[172:173], 11, v[168:169]
	v_lshl_add_u64 v[174:175], v[146:147], 1, s[18:19]
	v_lshl_add_u64 v[146:147], v[174:175], 0, v[172:173]
	s_waitcnt vmcnt(7)
	v_pk_mul_f32 v[128:129], v[128:129], v[176:177] op_sel_hi:[1,0]
	v_pk_mul_f32 v[126:127], v[126:127], v[176:177] op_sel_hi:[1,0]
	v_pk_mul_f32 v[124:125], v[124:125], v[176:177] op_sel_hi:[1,0]
	v_pk_mul_f32 v[122:123], v[122:123], v[176:177] op_sel_hi:[1,0]
	v_pk_mul_f32 v[120:121], v[120:121], v[176:177] op_sel_hi:[1,0]
	v_pk_mul_f32 v[118:119], v[118:119], v[176:177] op_sel_hi:[1,0]
	v_pk_mul_f32 v[172:173], v[112:113], v[176:177] op_sel_hi:[1,0]
	v_pk_mul_f32 v[170:171], v[110:111], v[176:177] op_sel_hi:[1,0]
	v_cvt_pk_bf16_f32 v110, v126, v127
	v_cvt_pk_bf16_f32 v111, v128, v129
	v_cvt_pk_bf16_f32 v112, v122, v123
	v_cvt_pk_bf16_f32 v113, v124, v125
	v_cvt_pk_bf16_f32 v118, v118, v119
	v_cvt_pk_bf16_f32 v119, v120, v121
	v_cvt_pk_bf16_f32 v120, v170, v171
	v_cvt_pk_bf16_f32 v121, v172, v173
	global_store_dwordx4 v[146:147], v[110:113], off
	global_store_dwordx4 v[146:147], v[118:121], off offset:256
	v_or_b32_e32 v112, 16, v168
	v_ashrrev_i32_e32 v113, 31, v112
	v_lshlrev_b64 v[112:113], 11, v[112:113]
	v_lshl_add_u64 v[112:113], v[174:175], 0, v[112:113]
	s_waitcnt vmcnt(8)
	v_pk_mul_f32 v[116:117], v[116:117], v[178:179] op_sel_hi:[1,0]
	v_pk_mul_f32 v[114:115], v[114:115], v[178:179] op_sel_hi:[1,0]
	v_pk_mul_f32 v[108:109], v[108:109], v[178:179] op_sel_hi:[1,0]
	v_pk_mul_f32 v[106:107], v[106:107], v[178:179] op_sel_hi:[1,0]
	v_pk_mul_f32 v[104:105], v[104:105], v[178:179] op_sel_hi:[1,0]
	v_pk_mul_f32 v[102:103], v[102:103], v[178:179] op_sel_hi:[1,0]
	v_pk_mul_f32 v[118:119], v[96:97], v[178:179] op_sel_hi:[1,0]
	v_pk_mul_f32 v[110:111], v[94:95], v[178:179] op_sel_hi:[1,0]
	v_cvt_pk_bf16_f32 v94, v114, v115
	v_cvt_pk_bf16_f32 v95, v116, v117
	v_cvt_pk_bf16_f32 v96, v106, v107
	v_cvt_pk_bf16_f32 v97, v108, v109
	v_cvt_pk_bf16_f32 v102, v102, v103
	v_cvt_pk_bf16_f32 v103, v104, v105
	v_cvt_pk_bf16_f32 v104, v110, v111
	v_cvt_pk_bf16_f32 v105, v118, v119
	global_store_dwordx4 v[112:113], v[94:97], off
	global_store_dwordx4 v[112:113], v[102:105], off offset:256
	v_or_b32_e32 v96, 32, v168
	v_ashrrev_i32_e32 v97, 31, v96
	v_lshlrev_b64 v[96:97], 11, v[96:97]
	v_lshl_add_u64 v[96:97], v[174:175], 0, v[96:97]
	s_waitcnt vmcnt(9)
	v_pk_mul_f32 v[100:101], v[100:101], v[180:181] op_sel_hi:[1,0]
	v_pk_mul_f32 v[98:99], v[98:99], v[180:181] op_sel_hi:[1,0]
	v_pk_mul_f32 v[92:93], v[92:93], v[180:181] op_sel_hi:[1,0]
	v_pk_mul_f32 v[90:91], v[90:91], v[180:181] op_sel_hi:[1,0]
	v_pk_mul_f32 v[88:89], v[88:89], v[180:181] op_sel_hi:[1,0]
	v_pk_mul_f32 v[86:87], v[86:87], v[180:181] op_sel_hi:[1,0]
	v_pk_mul_f32 v[102:103], v[80:81], v[180:181] op_sel_hi:[1,0]
	v_pk_mul_f32 v[94:95], v[78:79], v[180:181] op_sel_hi:[1,0]
	v_cvt_pk_bf16_f32 v78, v98, v99
	v_cvt_pk_bf16_f32 v79, v100, v101
	v_cvt_pk_bf16_f32 v80, v90, v91
	v_cvt_pk_bf16_f32 v81, v92, v93
	v_cvt_pk_bf16_f32 v86, v86, v87
	v_cvt_pk_bf16_f32 v87, v88, v89
	v_cvt_pk_bf16_f32 v88, v94, v95
	v_cvt_pk_bf16_f32 v89, v102, v103
	global_store_dwordx4 v[96:97], v[78:81], off
	global_store_dwordx4 v[96:97], v[86:89], off offset:256
	v_or_b32_e32 v80, 48, v168
	v_ashrrev_i32_e32 v81, 31, v80
	v_lshlrev_b64 v[80:81], 11, v[80:81]
	v_lshl_add_u64 v[80:81], v[174:175], 0, v[80:81]
	s_waitcnt vmcnt(10)
; __device__ __forceinline__ u32x4 pack8(const f32x4 a, const f32x4 b) { u32x4 w; w.x = cvt_pk_bf16(a[0], a[1]); w.y = cvt_pk_bf16(a[2], a[3]); w.z = cvt_pk_bf16(b[0], b[1]); w.w = cvt_pk_bf16(b[2], b[3]); return w; }
; #define PG8_BAR __builtin_amdgcn_s_barrier()
;     __device__ __forceinline__ void operator()(const f32x4 (&acc)[2][2][4][2], const Unit& u, int wr, int wc, int fr, int fq) const {
;     ...
; #pragma unroll
;         for (int ai = 0; ai < 2; ++ai)
; #pragma unroll
;             for (int m = 0; m < 4; ++m) { const int row = row0 + ai * HALF + m * 16; const float gsc = gvp[row];
; #pragma unroll
;                 for (int bj = 0; bj < 2; ++bj) *(u32x4*)(base + (size_t)row * D + col0 + bj * HALF) = pack8(acc[ai][bj][m][0] * gsc, acc[ai][bj][m][1] * gsc); }
;     ...
;         if (!has_next) break;
; #pragma unroll
;         for (int a = 0; a < 2; ++a)
; #pragma unroll
;             for (int b = 0; b < 2; ++b)
; #pragma unroll
;                 for (int m = 0; m < 4; ++m)
; #pragma unroll
;                     for (int n = 0; n < 2; ++n) acc[a][b][m][n] = (f32x4){0.f, 0.f, 0.f, 0.f};
;         cur = nxt; cA = nA; cB = nB; ++ui;
; #pragma unroll
;         for (int hh = 0; hh < 2; ++hh)
; #pragma unroll
;             for (int i = 0; i < 2; ++i) voffA[hh][i] = voffN[hh][i];
;         if (wr == 1) PG8_BAR;
	v_pk_mul_f32 v[84:85], v[84:85], v[182:183] op_sel_hi:[1,0]
	v_pk_mul_f32 v[82:83], v[82:83], v[182:183] op_sel_hi:[1,0]
	v_pk_mul_f32 v[76:77], v[76:77], v[182:183] op_sel_hi:[1,0]
	v_pk_mul_f32 v[74:75], v[74:75], v[182:183] op_sel_hi:[1,0]
	v_pk_mul_f32 v[72:73], v[72:73], v[182:183] op_sel_hi:[1,0]
	v_pk_mul_f32 v[70:71], v[70:71], v[182:183] op_sel_hi:[1,0]
	v_pk_mul_f32 v[86:87], v[68:69], v[182:183] op_sel_hi:[1,0]
	v_pk_mul_f32 v[78:79], v[66:67], v[182:183] op_sel_hi:[1,0]
	v_cvt_pk_bf16_f32 v66, v82, v83
	v_cvt_pk_bf16_f32 v67, v84, v85
	v_cvt_pk_bf16_f32 v68, v74, v75
	v_cvt_pk_bf16_f32 v69, v76, v77
	v_cvt_pk_bf16_f32 v70, v70, v71
	v_cvt_pk_bf16_f32 v71, v72, v73
	v_cvt_pk_bf16_f32 v72, v78, v79
	v_cvt_pk_bf16_f32 v73, v86, v87
	global_store_dwordx4 v[80:81], v[66:69], off
	global_store_dwordx4 v[80:81], v[70:73], off offset:256
	v_lshl_add_u64 v[68:69], v[146:147], 0, s[6:7]
	v_add_co_u32_e32 v70, vcc, s44, v146
	s_waitcnt vmcnt(11)
	v_pk_mul_f32 v[64:65], v[64:65], v[184:185] op_sel_hi:[1,0]
	v_pk_mul_f32 v[62:63], v[62:63], v[184:185] op_sel_hi:[1,0]
	v_pk_mul_f32 v[60:61], v[60:61], v[184:185] op_sel_hi:[1,0]
	v_pk_mul_f32 v[58:59], v[58:59], v[184:185] op_sel_hi:[1,0]
	v_addc_co_u32_e32 v71, vcc, 0, v147, vcc
	v_pk_mul_f32 v[56:57], v[56:57], v[184:185] op_sel_hi:[1,0]
	v_pk_mul_f32 v[54:55], v[54:55], v[184:185] op_sel_hi:[1,0]
	v_pk_mul_f32 v[72:73], v[52:53], v[184:185] op_sel_hi:[1,0]
	v_pk_mul_f32 v[66:67], v[50:51], v[184:185] op_sel_hi:[1,0]
	v_cvt_pk_bf16_f32 v50, v62, v63
	v_cvt_pk_bf16_f32 v51, v64, v65
	v_cvt_pk_bf16_f32 v52, v58, v59
	v_cvt_pk_bf16_f32 v53, v60, v61
	v_cvt_pk_bf16_f32 v54, v54, v55
	v_cvt_pk_bf16_f32 v55, v56, v57
	v_cvt_pk_bf16_f32 v56, v66, v67
	v_cvt_pk_bf16_f32 v57, v72, v73
	global_store_dwordx4 v[70:71], v[50:53], off
	global_store_dwordx4 v[68:69], v[54:57], off offset:256
	v_lshl_add_u64 v[52:53], v[146:147], 0, s[8:9]
	v_add_co_u32_e32 v54, vcc, s45, v146
	s_waitcnt vmcnt(12)
	v_pk_mul_f32 v[48:49], v[48:49], v[186:187] op_sel_hi:[1,0]
	v_pk_mul_f32 v[46:47], v[46:47], v[186:187] op_sel_hi:[1,0]
	v_pk_mul_f32 v[44:45], v[44:45], v[186:187] op_sel_hi:[1,0]
	v_pk_mul_f32 v[42:43], v[42:43], v[186:187] op_sel_hi:[1,0]
	v_addc_co_u32_e32 v55, vcc, 0, v147, vcc
	v_pk_mul_f32 v[40:41], v[40:41], v[186:187] op_sel_hi:[1,0]
	v_pk_mul_f32 v[38:39], v[38:39], v[186:187] op_sel_hi:[1,0]
	v_pk_mul_f32 v[56:57], v[36:37], v[186:187] op_sel_hi:[1,0]
	v_pk_mul_f32 v[50:51], v[34:35], v[186:187] op_sel_hi:[1,0]
	v_cvt_pk_bf16_f32 v34, v46, v47
	v_cvt_pk_bf16_f32 v35, v48, v49
	v_cvt_pk_bf16_f32 v36, v42, v43
	v_cvt_pk_bf16_f32 v37, v44, v45
	v_cvt_pk_bf16_f32 v38, v38, v39
	v_cvt_pk_bf16_f32 v39, v40, v41
	v_cvt_pk_bf16_f32 v40, v50, v51
	v_cvt_pk_bf16_f32 v41, v56, v57
	global_store_dwordx4 v[54:55], v[34:37], off
	global_store_dwordx4 v[52:53], v[38:41], off offset:256
	v_lshl_add_u64 v[36:37], v[146:147], 0, s[10:11]
	v_add_co_u32_e32 v38, vcc, s46, v146
	s_waitcnt vmcnt(13)
	v_pk_mul_f32 v[32:33], v[32:33], v[188:189] op_sel_hi:[1,0]
	v_pk_mul_f32 v[30:31], v[30:31], v[188:189] op_sel_hi:[1,0]
	v_pk_mul_f32 v[28:29], v[28:29], v[188:189] op_sel_hi:[1,0]
	v_pk_mul_f32 v[26:27], v[26:27], v[188:189] op_sel_hi:[1,0]
	v_addc_co_u32_e32 v39, vcc, 0, v147, vcc
	v_pk_mul_f32 v[24:25], v[24:25], v[188:189] op_sel_hi:[1,0]
	v_pk_mul_f32 v[22:23], v[22:23], v[188:189] op_sel_hi:[1,0]
	v_pk_mul_f32 v[40:41], v[20:21], v[188:189] op_sel_hi:[1,0]
	v_pk_mul_f32 v[34:35], v[18:19], v[188:189] op_sel_hi:[1,0]
	v_cvt_pk_bf16_f32 v18, v30, v31
	v_cvt_pk_bf16_f32 v19, v32, v33
	v_cvt_pk_bf16_f32 v20, v26, v27
	v_cvt_pk_bf16_f32 v21, v28, v29
	v_cvt_pk_bf16_f32 v22, v22, v23
	v_cvt_pk_bf16_f32 v23, v24, v25
	v_cvt_pk_bf16_f32 v24, v34, v35
	v_cvt_pk_bf16_f32 v25, v40, v41
	global_store_dwordx4 v[38:39], v[18:21], off
	global_store_dwordx4 v[36:37], v[22:25], off offset:256
	v_lshl_add_u64 v[20:21], v[146:147], 0, s[12:13]
	v_add_co_u32_e32 v22, vcc, s47, v146
	s_waitcnt vmcnt(14)
	v_pk_mul_f32 v[16:17], v[16:17], v[190:191] op_sel_hi:[1,0]
	v_addc_co_u32_e32 v23, vcc, 0, v147, vcc
	v_pk_mul_f32 v[14:15], v[14:15], v[190:191] op_sel_hi:[1,0]
	v_pk_mul_f32 v[12:13], v[12:13], v[190:191] op_sel_hi:[1,0]
	v_pk_mul_f32 v[10:11], v[10:11], v[190:191] op_sel_hi:[1,0]
	s_and_b64 vcc, exec, s[0:1]
	v_pk_mul_f32 v[8:9], v[8:9], v[190:191] op_sel_hi:[1,0]
	v_pk_mul_f32 v[6:7], v[6:7], v[190:191] op_sel_hi:[1,0]
	v_pk_mul_f32 v[24:25], v[4:5], v[190:191] op_sel_hi:[1,0]
	v_pk_mul_f32 v[18:19], v[2:3], v[190:191] op_sel_hi:[1,0]
	v_cvt_pk_bf16_f32 v2, v14, v15
	v_cvt_pk_bf16_f32 v3, v16, v17
	v_cvt_pk_bf16_f32 v4, v10, v11
	v_cvt_pk_bf16_f32 v5, v12, v13
	s_mov_b64 s[0:1], -1
	v_cvt_pk_bf16_f32 v6, v6, v7
	v_cvt_pk_bf16_f32 v7, v8, v9
	v_cvt_pk_bf16_f32 v8, v18, v19
	v_cvt_pk_bf16_f32 v9, v24, v25
	global_store_dwordx4 v[22:23], v[2:5], off
	global_store_dwordx4 v[20:21], v[6:9], off offset:256
	s_cbranch_vccnz .LBB0_2403
	s_andn2_b64 vcc, exec, s[2:3]
	s_cbranch_vccnz .LBB0_2402
	s_barrier
	s_branch .LBB0_2402
